# speedup vs baseline: 1.0331x; 1.0002x over previous
.LBB3_11:
	s_lshl_b32 s58, s42, 7
	s_add_i32 s59, s41, 0x400
	s_lshr_b32 s59, s59, 6
	s_bfe_u32 s60, s20, 0x1000c
	s_add_i32 s59, s59, s60
	s_lshl_b32 s59, s59, 19
	s_add_u32 s58, s58, s59
	s_add_u32 s58, s56, s58
	s_addc_u32 s59, s57, 0
	s_add_u32 s60, s58, 0x4000
	s_addc_u32 s61, s59, 0
	s_add_u32 s62, s58, 0x100000
	s_addc_u32 s63, s59, 0
	s_add_u32 s64, s62, 0x4000
	s_addc_u32 s65, s63, 0
	s_lshr_b32 s66, s41, 7
	s_bfe_u32 s67, s20, 0x1000c
	s_add_i32 s66, s66, s67
	s_lshl_b32 s66, s66, 14
	s_lshl_b32 s67, s42, 2
	s_add_u32 s66, s66, s67
	s_add_u32 s66, s14, s66
	s_addc_u32 s67, s15, 0
	v_add_u32_e32 v172, s43, v207
	v_exp_f32_e32 v130, v114
	v_exp_f32_e32 v131, v115
	v_exp_f32_e32 v132, v116
	v_exp_f32_e32 v133, v117
	v_exp_f32_e32 v142, v78
	v_exp_f32_e32 v143, v79
	v_exp_f32_e32 v144, v80
	v_exp_f32_e32 v145, v81
	v_exp_f32_e32 v176, v106
	v_exp_f32_e32 v177, v107
	v_exp_f32_e32 v178, v108
	v_exp_f32_e32 v179, v109
	v_exp_f32_e32 v232, v70
	v_exp_f32_e32 v233, v71
	v_exp_f32_e32 v234, v72
	v_exp_f32_e32 v235, v73
	v_pk_add_f32 v[130:131], v[130:131], 1.0 op_sel_hi:[1,0]
	v_pk_add_f32 v[132:133], v[132:133], 1.0 op_sel_hi:[1,0]
	v_pk_add_f32 v[142:143], v[142:143], 1.0 op_sel_hi:[1,0]
	v_pk_add_f32 v[144:145], v[144:145], 1.0 op_sel_hi:[1,0]
	v_pk_add_f32 v[176:177], v[176:177], 1.0 op_sel_hi:[1,0]
	v_pk_add_f32 v[178:179], v[178:179], 1.0 op_sel_hi:[1,0]
	v_pk_add_f32 v[232:233], v[232:233], 1.0 op_sel_hi:[1,0]
	v_pk_add_f32 v[234:235], v[234:235], 1.0 op_sel_hi:[1,0]
	v_pk_mul_f32 v[134:135], v[130:131], v[132:133]
	v_pk_mul_f32 v[146:147], v[142:143], v[144:145]
	v_pk_mul_f32 v[180:181], v[176:177], v[178:179]
	v_pk_mul_f32 v[236:237], v[232:233], v[234:235]
	v_rcp_f32_e64 v136, -v134
	v_rcp_f32_e64 v137, -v135
	v_rcp_f32_e64 v148, -v146
	v_rcp_f32_e64 v149, -v147
	v_rcp_f32_e64 v182, -v180
	v_rcp_f32_e64 v183, -v181
	v_rcp_f32_e64 v238, -v236
	v_rcp_f32_e64 v239, -v237
	v_pk_add_f32 v[164:165], v[114:115], v[116:117]
	v_pk_add_f32 v[164:165], v[164:165], v[78:79]
	v_pk_add_f32 v[164:165], v[164:165], v[80:81]
	v_pk_add_f32 v[164:165], v[164:165], v[106:107]
	v_pk_add_f32 v[164:165], v[164:165], v[108:109]
	v_pk_add_f32 v[164:165], v[164:165], v[70:71]
	v_pk_add_f32 v[164:165], v[164:165], v[72:73]
	v_pk_mul_f32 v[162:163], v[134:135], v[146:147]
	v_pk_mul_f32 v[162:163], v[162:163], v[180:181]
	v_pk_mul_f32 v[162:163], v[162:163], v[236:237]
	v_pk_mul_f32 v[140:141], v[136:137], v[130:131]
	v_pk_mul_f32 v[138:139], v[136:137], v[132:133]
	v_pk_mul_f32 v[152:153], v[148:149], v[142:143]
	v_pk_mul_f32 v[150:151], v[148:149], v[144:145]
	v_pk_mul_f32 v[186:187], v[182:183], v[176:177]
	v_pk_mul_f32 v[184:185], v[182:183], v[178:179]
	v_pk_mul_f32 v[242:243], v[238:239], v[232:233]
	v_pk_mul_f32 v[240:241], v[238:239], v[234:235]
	v_pk_fma_f32 v[138:139], v[138:139], 2.0, 1.0 op_sel_hi:[1,0,0]
	v_pk_fma_f32 v[140:141], v[140:141], 2.0, 1.0 op_sel_hi:[1,0,0]
	v_pk_fma_f32 v[150:151], v[150:151], 2.0, 1.0 op_sel_hi:[1,0,0]
	v_pk_fma_f32 v[152:153], v[152:153], 2.0, 1.0 op_sel_hi:[1,0,0]
	v_pk_fma_f32 v[184:185], v[184:185], 2.0, 1.0 op_sel_hi:[1,0,0]
	v_pk_fma_f32 v[186:187], v[186:187], 2.0, 1.0 op_sel_hi:[1,0,0]
	v_pk_fma_f32 v[240:241], v[240:241], 2.0, 1.0 op_sel_hi:[1,0,0]
	v_pk_fma_f32 v[242:243], v[242:243], 2.0, 1.0 op_sel_hi:[1,0,0]
	v_cvt_pk_bf16_f32 v154, v138, v139
	v_cvt_pk_bf16_f32 v155, v140, v141
	v_cvt_pk_bf16_f32 v156, v150, v151
	v_cvt_pk_bf16_f32 v157, v152, v153
	v_cvt_pk_bf16_f32 v158, v184, v185
	v_cvt_pk_bf16_f32 v159, v186, v187
	v_cvt_pk_bf16_f32 v160, v240, v241
	v_cvt_pk_bf16_f32 v161, v242, v243
	ds_read_b128 v[114:117], v172
	ds_read_b128 v[78:81], v172 offset:64
	ds_read_b128 v[106:109], v172 offset:128
	ds_read_b128 v[70:73], v172 offset:192
	v_permlane16_swap_b32_e32 v154, v156
	v_permlane16_swap_b32_e32 v155, v157
	global_store_dwordx4 v228, v[154:157], s[58:59] nt
	s_bitcmp1_b32 s20, 12
	s_cbranch_scc1 .Lg1_noX
	s_barrier
.Lg1_noX:
	v_permlane16_swap_b32_e32 v158, v160
	v_permlane16_swap_b32_e32 v159, v161
	global_store_dwordx4 v228, v[158:161], s[58:59] offset:128 nt
	v_exp_f32_e32 v130, v90
	v_exp_f32_e32 v131, v91
	v_exp_f32_e32 v132, v92
	v_exp_f32_e32 v133, v93
	v_exp_f32_e32 v142, v42
	v_exp_f32_e32 v143, v43
	v_exp_f32_e32 v144, v44
	v_exp_f32_e32 v145, v45
	v_exp_f32_e32 v176, v126
	v_exp_f32_e32 v177, v127
	v_exp_f32_e32 v178, v128
	v_exp_f32_e32 v179, v129
	v_exp_f32_e32 v232, v58
	v_exp_f32_e32 v233, v59
	v_exp_f32_e32 v234, v60
	v_exp_f32_e32 v235, v61
	v_pk_add_f32 v[130:131], v[130:131], 1.0 op_sel_hi:[1,0]
	v_pk_add_f32 v[132:133], v[132:133], 1.0 op_sel_hi:[1,0]
	v_pk_add_f32 v[142:143], v[142:143], 1.0 op_sel_hi:[1,0]
	v_pk_add_f32 v[144:145], v[144:145], 1.0 op_sel_hi:[1,0]
	v_pk_add_f32 v[176:177], v[176:177], 1.0 op_sel_hi:[1,0]
	v_pk_add_f32 v[178:179], v[178:179], 1.0 op_sel_hi:[1,0]
	v_pk_add_f32 v[232:233], v[232:233], 1.0 op_sel_hi:[1,0]
	v_pk_add_f32 v[234:235], v[234:235], 1.0 op_sel_hi:[1,0]
	v_pk_mul_f32 v[134:135], v[130:131], v[132:133]
	v_pk_mul_f32 v[146:147], v[142:143], v[144:145]
	v_pk_mul_f32 v[180:181], v[176:177], v[178:179]
	v_pk_mul_f32 v[236:237], v[232:233], v[234:235]
	v_rcp_f32_e64 v136, -v134
	v_rcp_f32_e64 v137, -v135
	v_rcp_f32_e64 v148, -v146
	v_rcp_f32_e64 v149, -v147
	v_rcp_f32_e64 v182, -v180
	v_rcp_f32_e64 v183, -v181
	v_rcp_f32_e64 v238, -v236
	v_rcp_f32_e64 v239, -v237
	v_pk_add_f32 v[164:165], v[164:165], v[90:91]
	v_pk_add_f32 v[164:165], v[164:165], v[92:93]
	v_pk_add_f32 v[164:165], v[164:165], v[42:43]
	v_pk_add_f32 v[164:165], v[164:165], v[44:45]
	v_pk_add_f32 v[164:165], v[164:165], v[126:127]
	v_pk_add_f32 v[164:165], v[164:165], v[128:129]
	v_pk_add_f32 v[164:165], v[164:165], v[58:59]
	v_pk_add_f32 v[164:165], v[164:165], v[60:61]
	v_pk_mul_f32 v[174:175], v[134:135], v[146:147]
	v_pk_mul_f32 v[174:175], v[174:175], v[180:181]
	v_pk_mul_f32 v[174:175], v[174:175], v[236:237]
	v_pk_mul_f32 v[140:141], v[136:137], v[130:131]
	v_pk_mul_f32 v[138:139], v[136:137], v[132:133]
	v_pk_mul_f32 v[152:153], v[148:149], v[142:143]
	v_pk_mul_f32 v[150:151], v[148:149], v[144:145]
	v_pk_mul_f32 v[186:187], v[182:183], v[176:177]
	v_pk_mul_f32 v[184:185], v[182:183], v[178:179]
	v_pk_mul_f32 v[242:243], v[238:239], v[232:233]
	v_pk_mul_f32 v[240:241], v[238:239], v[234:235]
	v_pk_fma_f32 v[138:139], v[138:139], 2.0, 1.0 op_sel_hi:[1,0,0]
	v_pk_fma_f32 v[140:141], v[140:141], 2.0, 1.0 op_sel_hi:[1,0,0]
	v_pk_fma_f32 v[150:151], v[150:151], 2.0, 1.0 op_sel_hi:[1,0,0]
	v_pk_fma_f32 v[152:153], v[152:153], 2.0, 1.0 op_sel_hi:[1,0,0]
	v_pk_fma_f32 v[184:185], v[184:185], 2.0, 1.0 op_sel_hi:[1,0,0]
	v_pk_fma_f32 v[186:187], v[186:187], 2.0, 1.0 op_sel_hi:[1,0,0]
	v_pk_fma_f32 v[240:241], v[240:241], 2.0, 1.0 op_sel_hi:[1,0,0]
	v_pk_fma_f32 v[242:243], v[242:243], 2.0, 1.0 op_sel_hi:[1,0,0]
	v_cvt_pk_bf16_f32 v154, v138, v139
	v_cvt_pk_bf16_f32 v155, v140, v141
	v_cvt_pk_bf16_f32 v156, v150, v151
	v_cvt_pk_bf16_f32 v157, v152, v153
	v_cvt_pk_bf16_f32 v158, v184, v185
	v_cvt_pk_bf16_f32 v159, v186, v187
	v_cvt_pk_bf16_f32 v160, v240, v241
	v_cvt_pk_bf16_f32 v161, v242, v243
	ds_read_b128 v[90:93], v172 offset:512
	ds_read_b128 v[42:45], v172 offset:576
	ds_read_b128 v[126:129], v172 offset:640
	ds_read_b128 v[58:61], v172 offset:704
	v_permlane16_swap_b32_e32 v154, v156
	v_permlane16_swap_b32_e32 v155, v157
	global_store_dwordx4 v228, v[154:157], s[62:63] nt
	v_permlane16_swap_b32_e32 v158, v160
	v_permlane16_swap_b32_e32 v159, v161
	global_store_dwordx4 v228, v[158:161], s[62:63] offset:128 nt
	v_log_f32_e32 v166, v162
	v_log_f32_e32 v167, v163
	v_log_f32_e32 v170, v174
	v_log_f32_e32 v171, v175
	v_add_f32_e32 v168, v164, v165
	v_mul_f32_e32 v168, 0xbeb17218, v168
	v_add_f32_e32 v166, v166, v167
	v_add_f32_e32 v170, v170, v171
	v_add_f32_e32 v166, v166, v170
	v_add_f32_e32 v166, 0xc2000000, v166
	v_fmac_f32_e32 v168, 0x3f317218, v166
	v_mov_b32_e32 v169, v168
	s_nop 1
	v_permlane16_swap_b32_e32 v168, v169
	v_add_f32_e32 v168, v168, v169
	v_mov_b32_e32 v169, v168
	s_nop 1
	v_permlane32_swap_b32_e32 v168, v169
	v_add_f32_e32 v168, v168, v169
	s_mov_b64 exec, s[0:1]
	global_store_dword v229, v168, s[66:67]
	s_mov_b64 exec, -1
	v_exp_f32_e32 v130, v110
	v_exp_f32_e32 v131, v111
	v_exp_f32_e32 v132, v112
	v_exp_f32_e32 v133, v113
	v_exp_f32_e32 v142, v74
	v_exp_f32_e32 v143, v75
	v_exp_f32_e32 v144, v76
	v_exp_f32_e32 v145, v77
	v_exp_f32_e32 v176, v102
	v_exp_f32_e32 v177, v103
	v_exp_f32_e32 v178, v104
	v_exp_f32_e32 v179, v105
	v_exp_f32_e32 v232, v66
	v_exp_f32_e32 v233, v67
	v_exp_f32_e32 v234, v68
	v_exp_f32_e32 v235, v69
	v_pk_add_f32 v[130:131], v[130:131], 1.0 op_sel_hi:[1,0]
	v_pk_add_f32 v[132:133], v[132:133], 1.0 op_sel_hi:[1,0]
	v_pk_add_f32 v[142:143], v[142:143], 1.0 op_sel_hi:[1,0]
	v_pk_add_f32 v[144:145], v[144:145], 1.0 op_sel_hi:[1,0]
	v_pk_add_f32 v[176:177], v[176:177], 1.0 op_sel_hi:[1,0]
	v_pk_add_f32 v[178:179], v[178:179], 1.0 op_sel_hi:[1,0]
	v_pk_add_f32 v[232:233], v[232:233], 1.0 op_sel_hi:[1,0]
	v_pk_add_f32 v[234:235], v[234:235], 1.0 op_sel_hi:[1,0]
	v_pk_mul_f32 v[134:135], v[130:131], v[132:133]
	v_pk_mul_f32 v[146:147], v[142:143], v[144:145]
	v_pk_mul_f32 v[180:181], v[176:177], v[178:179]
	v_pk_mul_f32 v[236:237], v[232:233], v[234:235]
	v_rcp_f32_e64 v136, -v134
	v_rcp_f32_e64 v137, -v135
	v_rcp_f32_e64 v148, -v146
	v_rcp_f32_e64 v149, -v147
	v_rcp_f32_e64 v182, -v180
	v_rcp_f32_e64 v183, -v181
	v_rcp_f32_e64 v238, -v236
	v_rcp_f32_e64 v239, -v237
	v_pk_add_f32 v[164:165], v[110:111], v[112:113]
	v_pk_add_f32 v[164:165], v[164:165], v[74:75]
	v_pk_add_f32 v[164:165], v[164:165], v[76:77]
	v_pk_add_f32 v[164:165], v[164:165], v[102:103]
	v_pk_add_f32 v[164:165], v[164:165], v[104:105]
	v_pk_add_f32 v[164:165], v[164:165], v[66:67]
	v_pk_add_f32 v[164:165], v[164:165], v[68:69]
	v_pk_mul_f32 v[162:163], v[134:135], v[146:147]
	v_pk_mul_f32 v[162:163], v[162:163], v[180:181]
	v_pk_mul_f32 v[162:163], v[162:163], v[236:237]
	v_pk_mul_f32 v[140:141], v[136:137], v[130:131]
	v_pk_mul_f32 v[138:139], v[136:137], v[132:133]
	v_pk_mul_f32 v[152:153], v[148:149], v[142:143]
	v_pk_mul_f32 v[150:151], v[148:149], v[144:145]
	v_pk_mul_f32 v[186:187], v[182:183], v[176:177]
	v_pk_mul_f32 v[184:185], v[182:183], v[178:179]
	v_pk_mul_f32 v[242:243], v[238:239], v[232:233]
	v_pk_mul_f32 v[240:241], v[238:239], v[234:235]
	v_pk_fma_f32 v[138:139], v[138:139], 2.0, 1.0 op_sel_hi:[1,0,0]
	v_pk_fma_f32 v[140:141], v[140:141], 2.0, 1.0 op_sel_hi:[1,0,0]
	v_pk_fma_f32 v[150:151], v[150:151], 2.0, 1.0 op_sel_hi:[1,0,0]
	v_pk_fma_f32 v[152:153], v[152:153], 2.0, 1.0 op_sel_hi:[1,0,0]
	v_pk_fma_f32 v[184:185], v[184:185], 2.0, 1.0 op_sel_hi:[1,0,0]
	v_pk_fma_f32 v[186:187], v[186:187], 2.0, 1.0 op_sel_hi:[1,0,0]
	v_pk_fma_f32 v[240:241], v[240:241], 2.0, 1.0 op_sel_hi:[1,0,0]
	v_pk_fma_f32 v[242:243], v[242:243], 2.0, 1.0 op_sel_hi:[1,0,0]
	v_cvt_pk_bf16_f32 v154, v138, v139
	v_cvt_pk_bf16_f32 v155, v140, v141
	v_cvt_pk_bf16_f32 v156, v150, v151
	v_cvt_pk_bf16_f32 v157, v152, v153
	v_cvt_pk_bf16_f32 v158, v184, v185
	v_cvt_pk_bf16_f32 v159, v186, v187
	v_cvt_pk_bf16_f32 v160, v240, v241
	v_cvt_pk_bf16_f32 v161, v242, v243
	ds_read_b128 v[110:113], v172
	ds_read_b128 v[74:77], v172 offset:64
	ds_read_b128 v[102:105], v172 offset:128
	ds_read_b128 v[66:69], v172 offset:192
	v_permlane16_swap_b32_e32 v154, v156
	v_permlane16_swap_b32_e32 v155, v157
	global_store_dwordx4 v228, v[154:157], s[58:59] offset:2048 nt
	v_permlane16_swap_b32_e32 v158, v160
	v_permlane16_swap_b32_e32 v159, v161
	global_store_dwordx4 v228, v[158:161], s[58:59] offset:2176 nt
	v_exp_f32_e32 v130, v86
	v_exp_f32_e32 v131, v87
	v_exp_f32_e32 v132, v88
	v_exp_f32_e32 v133, v89
	v_exp_f32_e32 v142, v38
	v_exp_f32_e32 v143, v39
	v_exp_f32_e32 v144, v40
	v_exp_f32_e32 v145, v41
	v_exp_f32_e32 v176, v122
	v_exp_f32_e32 v177, v123
	v_exp_f32_e32 v178, v124
	v_exp_f32_e32 v179, v125
	v_exp_f32_e32 v232, v50
	v_exp_f32_e32 v233, v51
	v_exp_f32_e32 v234, v52
	v_exp_f32_e32 v235, v53
	v_pk_add_f32 v[130:131], v[130:131], 1.0 op_sel_hi:[1,0]
	v_pk_add_f32 v[132:133], v[132:133], 1.0 op_sel_hi:[1,0]
	v_pk_add_f32 v[142:143], v[142:143], 1.0 op_sel_hi:[1,0]
	v_pk_add_f32 v[144:145], v[144:145], 1.0 op_sel_hi:[1,0]
	v_pk_add_f32 v[176:177], v[176:177], 1.0 op_sel_hi:[1,0]
	v_pk_add_f32 v[178:179], v[178:179], 1.0 op_sel_hi:[1,0]
	v_pk_add_f32 v[232:233], v[232:233], 1.0 op_sel_hi:[1,0]
	v_pk_add_f32 v[234:235], v[234:235], 1.0 op_sel_hi:[1,0]
	v_pk_mul_f32 v[134:135], v[130:131], v[132:133]
	v_pk_mul_f32 v[146:147], v[142:143], v[144:145]
	v_pk_mul_f32 v[180:181], v[176:177], v[178:179]
	v_pk_mul_f32 v[236:237], v[232:233], v[234:235]
	v_rcp_f32_e64 v136, -v134
	v_rcp_f32_e64 v137, -v135
	v_rcp_f32_e64 v148, -v146
	v_rcp_f32_e64 v149, -v147
	v_rcp_f32_e64 v182, -v180
	v_rcp_f32_e64 v183, -v181
	v_rcp_f32_e64 v238, -v236
	v_rcp_f32_e64 v239, -v237
	v_pk_add_f32 v[164:165], v[164:165], v[86:87]
	v_pk_add_f32 v[164:165], v[164:165], v[88:89]
	v_pk_add_f32 v[164:165], v[164:165], v[38:39]
	v_pk_add_f32 v[164:165], v[164:165], v[40:41]
	v_pk_add_f32 v[164:165], v[164:165], v[122:123]
	v_pk_add_f32 v[164:165], v[164:165], v[124:125]
	v_pk_add_f32 v[164:165], v[164:165], v[50:51]
	v_pk_add_f32 v[164:165], v[164:165], v[52:53]
	v_pk_mul_f32 v[174:175], v[134:135], v[146:147]
	v_pk_mul_f32 v[174:175], v[174:175], v[180:181]
	v_pk_mul_f32 v[174:175], v[174:175], v[236:237]
	v_pk_mul_f32 v[140:141], v[136:137], v[130:131]
	v_pk_mul_f32 v[138:139], v[136:137], v[132:133]
	v_pk_mul_f32 v[152:153], v[148:149], v[142:143]
	v_pk_mul_f32 v[150:151], v[148:149], v[144:145]
	v_pk_mul_f32 v[186:187], v[182:183], v[176:177]
	v_pk_mul_f32 v[184:185], v[182:183], v[178:179]
	v_pk_mul_f32 v[242:243], v[238:239], v[232:233]
	v_pk_mul_f32 v[240:241], v[238:239], v[234:235]
	v_pk_fma_f32 v[138:139], v[138:139], 2.0, 1.0 op_sel_hi:[1,0,0]
	v_pk_fma_f32 v[140:141], v[140:141], 2.0, 1.0 op_sel_hi:[1,0,0]
	v_pk_fma_f32 v[150:151], v[150:151], 2.0, 1.0 op_sel_hi:[1,0,0]
	v_pk_fma_f32 v[152:153], v[152:153], 2.0, 1.0 op_sel_hi:[1,0,0]
	v_pk_fma_f32 v[184:185], v[184:185], 2.0, 1.0 op_sel_hi:[1,0,0]
	v_pk_fma_f32 v[186:187], v[186:187], 2.0, 1.0 op_sel_hi:[1,0,0]
	v_pk_fma_f32 v[240:241], v[240:241], 2.0, 1.0 op_sel_hi:[1,0,0]
	v_pk_fma_f32 v[242:243], v[242:243], 2.0, 1.0 op_sel_hi:[1,0,0]
	v_cvt_pk_bf16_f32 v154, v138, v139
	v_cvt_pk_bf16_f32 v155, v140, v141
	v_cvt_pk_bf16_f32 v156, v150, v151
	v_cvt_pk_bf16_f32 v157, v152, v153
	v_cvt_pk_bf16_f32 v158, v184, v185
	v_cvt_pk_bf16_f32 v159, v186, v187
	v_cvt_pk_bf16_f32 v160, v240, v241
	v_cvt_pk_bf16_f32 v161, v242, v243
	ds_read_b128 v[86:89], v172 offset:512
	ds_read_b128 v[38:41], v172 offset:576
	ds_read_b128 v[122:125], v172 offset:640
	ds_read_b128 v[50:53], v172 offset:704
	v_permlane16_swap_b32_e32 v154, v156
	v_permlane16_swap_b32_e32 v155, v157
	global_store_dwordx4 v228, v[154:157], s[62:63] offset:2048 nt
	v_permlane16_swap_b32_e32 v158, v160
	v_permlane16_swap_b32_e32 v159, v161
	global_store_dwordx4 v228, v[158:161], s[62:63] offset:2176 nt
	v_log_f32_e32 v166, v162
	v_log_f32_e32 v167, v163
	v_log_f32_e32 v170, v174
	v_log_f32_e32 v171, v175
	v_add_f32_e32 v168, v164, v165
	v_mul_f32_e32 v168, 0xbeb17218, v168
	v_add_f32_e32 v166, v166, v167
	v_add_f32_e32 v170, v170, v171
	v_add_f32_e32 v166, v166, v170
	v_add_f32_e32 v166, 0xc2000000, v166
	v_fmac_f32_e32 v168, 0x3f317218, v166
	v_mov_b32_e32 v169, v168
	s_nop 1
	v_permlane16_swap_b32_e32 v168, v169
	v_add_f32_e32 v168, v168, v169
	v_mov_b32_e32 v169, v168
	s_nop 1
	v_permlane32_swap_b32_e32 v168, v169
	v_add_f32_e32 v168, v168, v169
	s_mov_b64 exec, s[0:1]
	global_store_dword v229, v168, s[66:67] offset:64
	s_mov_b64 exec, -1
	v_exp_f32_e32 v130, v98
	v_exp_f32_e32 v131, v99
	v_exp_f32_e32 v132, v100
	v_exp_f32_e32 v133, v101
	v_exp_f32_e32 v142, v62
	v_exp_f32_e32 v143, v63
	v_exp_f32_e32 v144, v64
	v_exp_f32_e32 v145, v65
	v_exp_f32_e32 v176, v94
	v_exp_f32_e32 v177, v95
	v_exp_f32_e32 v178, v96
	v_exp_f32_e32 v179, v97
	v_exp_f32_e32 v232, v54
	v_exp_f32_e32 v233, v55
	v_exp_f32_e32 v234, v56
	v_exp_f32_e32 v235, v57
	v_pk_add_f32 v[130:131], v[130:131], 1.0 op_sel_hi:[1,0]
	v_pk_add_f32 v[132:133], v[132:133], 1.0 op_sel_hi:[1,0]
	v_pk_add_f32 v[142:143], v[142:143], 1.0 op_sel_hi:[1,0]
	v_pk_add_f32 v[144:145], v[144:145], 1.0 op_sel_hi:[1,0]
	v_pk_add_f32 v[176:177], v[176:177], 1.0 op_sel_hi:[1,0]
	v_pk_add_f32 v[178:179], v[178:179], 1.0 op_sel_hi:[1,0]
	v_pk_add_f32 v[232:233], v[232:233], 1.0 op_sel_hi:[1,0]
	v_pk_add_f32 v[234:235], v[234:235], 1.0 op_sel_hi:[1,0]
	v_pk_mul_f32 v[134:135], v[130:131], v[132:133]
	v_pk_mul_f32 v[146:147], v[142:143], v[144:145]
	v_pk_mul_f32 v[180:181], v[176:177], v[178:179]
	v_pk_mul_f32 v[236:237], v[232:233], v[234:235]
	v_rcp_f32_e64 v136, -v134
	v_rcp_f32_e64 v137, -v135
	v_rcp_f32_e64 v148, -v146
	v_rcp_f32_e64 v149, -v147
	v_rcp_f32_e64 v182, -v180
	v_rcp_f32_e64 v183, -v181
	v_rcp_f32_e64 v238, -v236
	v_rcp_f32_e64 v239, -v237
	v_pk_add_f32 v[164:165], v[98:99], v[100:101]
	v_pk_add_f32 v[164:165], v[164:165], v[62:63]
	v_pk_add_f32 v[164:165], v[164:165], v[64:65]
	v_pk_add_f32 v[164:165], v[164:165], v[94:95]
	v_pk_add_f32 v[164:165], v[164:165], v[96:97]
	v_pk_add_f32 v[164:165], v[164:165], v[54:55]
	v_pk_add_f32 v[164:165], v[164:165], v[56:57]
	v_pk_mul_f32 v[162:163], v[134:135], v[146:147]
	v_pk_mul_f32 v[162:163], v[162:163], v[180:181]
	v_pk_mul_f32 v[162:163], v[162:163], v[236:237]
	v_pk_mul_f32 v[140:141], v[136:137], v[130:131]
	v_pk_mul_f32 v[138:139], v[136:137], v[132:133]
	v_pk_mul_f32 v[152:153], v[148:149], v[142:143]
	v_pk_mul_f32 v[150:151], v[148:149], v[144:145]
	v_pk_mul_f32 v[186:187], v[182:183], v[176:177]
	v_pk_mul_f32 v[184:185], v[182:183], v[178:179]
	v_pk_mul_f32 v[242:243], v[238:239], v[232:233]
	v_pk_mul_f32 v[240:241], v[238:239], v[234:235]
	v_pk_fma_f32 v[138:139], v[138:139], 2.0, 1.0 op_sel_hi:[1,0,0]
	v_pk_fma_f32 v[140:141], v[140:141], 2.0, 1.0 op_sel_hi:[1,0,0]
	v_pk_fma_f32 v[150:151], v[150:151], 2.0, 1.0 op_sel_hi:[1,0,0]
	v_pk_fma_f32 v[152:153], v[152:153], 2.0, 1.0 op_sel_hi:[1,0,0]
	v_pk_fma_f32 v[184:185], v[184:185], 2.0, 1.0 op_sel_hi:[1,0,0]
	v_pk_fma_f32 v[186:187], v[186:187], 2.0, 1.0 op_sel_hi:[1,0,0]
	v_pk_fma_f32 v[240:241], v[240:241], 2.0, 1.0 op_sel_hi:[1,0,0]
	v_pk_fma_f32 v[242:243], v[242:243], 2.0, 1.0 op_sel_hi:[1,0,0]
	v_cvt_pk_bf16_f32 v154, v138, v139
	v_cvt_pk_bf16_f32 v155, v140, v141
	v_cvt_pk_bf16_f32 v156, v150, v151
	v_cvt_pk_bf16_f32 v157, v152, v153
	v_cvt_pk_bf16_f32 v158, v184, v185
	v_cvt_pk_bf16_f32 v159, v186, v187
	v_cvt_pk_bf16_f32 v160, v240, v241
	v_cvt_pk_bf16_f32 v161, v242, v243
	ds_read_b128 v[98:101], v172
	ds_read_b128 v[62:65], v172 offset:64
	ds_read_b128 v[94:97], v172 offset:128
	ds_read_b128 v[54:57], v172 offset:192
	v_permlane16_swap_b32_e32 v154, v156
	v_permlane16_swap_b32_e32 v155, v157
	global_store_dwordx4 v228, v[154:157], s[60:61] nt
	v_permlane16_swap_b32_e32 v158, v160
	v_permlane16_swap_b32_e32 v159, v161
	global_store_dwordx4 v228, v[158:161], s[60:61] offset:128 nt
	v_exp_f32_e32 v130, v82
	v_exp_f32_e32 v131, v83
	v_exp_f32_e32 v132, v84
	v_exp_f32_e32 v133, v85
	v_exp_f32_e32 v142, v34
	v_exp_f32_e32 v143, v35
	v_exp_f32_e32 v144, v36
	v_exp_f32_e32 v145, v37
	v_exp_f32_e32 v176, v118
	v_exp_f32_e32 v177, v119
	v_exp_f32_e32 v178, v120
	v_exp_f32_e32 v179, v121
	v_exp_f32_e32 v232, v46
	v_exp_f32_e32 v233, v47
	v_exp_f32_e32 v234, v48
	v_exp_f32_e32 v235, v49
	v_pk_add_f32 v[130:131], v[130:131], 1.0 op_sel_hi:[1,0]
	v_pk_add_f32 v[132:133], v[132:133], 1.0 op_sel_hi:[1,0]
	v_pk_add_f32 v[142:143], v[142:143], 1.0 op_sel_hi:[1,0]
	v_pk_add_f32 v[144:145], v[144:145], 1.0 op_sel_hi:[1,0]
	v_pk_add_f32 v[176:177], v[176:177], 1.0 op_sel_hi:[1,0]
	v_pk_add_f32 v[178:179], v[178:179], 1.0 op_sel_hi:[1,0]
	v_pk_add_f32 v[232:233], v[232:233], 1.0 op_sel_hi:[1,0]
	v_pk_add_f32 v[234:235], v[234:235], 1.0 op_sel_hi:[1,0]
	v_pk_mul_f32 v[134:135], v[130:131], v[132:133]
	v_pk_mul_f32 v[146:147], v[142:143], v[144:145]
	v_pk_mul_f32 v[180:181], v[176:177], v[178:179]
	v_pk_mul_f32 v[236:237], v[232:233], v[234:235]
	v_rcp_f32_e64 v136, -v134
	v_rcp_f32_e64 v137, -v135
	v_rcp_f32_e64 v148, -v146
	v_rcp_f32_e64 v149, -v147
	v_rcp_f32_e64 v182, -v180
	v_rcp_f32_e64 v183, -v181
	v_rcp_f32_e64 v238, -v236
	v_rcp_f32_e64 v239, -v237
	v_pk_add_f32 v[164:165], v[164:165], v[82:83]
	v_pk_add_f32 v[164:165], v[164:165], v[84:85]
	v_pk_add_f32 v[164:165], v[164:165], v[34:35]
	v_pk_add_f32 v[164:165], v[164:165], v[36:37]
	v_pk_add_f32 v[164:165], v[164:165], v[118:119]
	v_pk_add_f32 v[164:165], v[164:165], v[120:121]
	v_pk_add_f32 v[164:165], v[164:165], v[46:47]
	v_pk_add_f32 v[164:165], v[164:165], v[48:49]
	v_pk_mul_f32 v[174:175], v[134:135], v[146:147]
	v_pk_mul_f32 v[174:175], v[174:175], v[180:181]
	v_pk_mul_f32 v[174:175], v[174:175], v[236:237]
	v_pk_mul_f32 v[140:141], v[136:137], v[130:131]
	v_pk_mul_f32 v[138:139], v[136:137], v[132:133]
	v_pk_mul_f32 v[152:153], v[148:149], v[142:143]
	v_pk_mul_f32 v[150:151], v[148:149], v[144:145]
	v_pk_mul_f32 v[186:187], v[182:183], v[176:177]
	v_pk_mul_f32 v[184:185], v[182:183], v[178:179]
	v_pk_mul_f32 v[242:243], v[238:239], v[232:233]
	v_pk_mul_f32 v[240:241], v[238:239], v[234:235]
	v_pk_fma_f32 v[138:139], v[138:139], 2.0, 1.0 op_sel_hi:[1,0,0]
	v_pk_fma_f32 v[140:141], v[140:141], 2.0, 1.0 op_sel_hi:[1,0,0]
	v_pk_fma_f32 v[150:151], v[150:151], 2.0, 1.0 op_sel_hi:[1,0,0]
	v_pk_fma_f32 v[152:153], v[152:153], 2.0, 1.0 op_sel_hi:[1,0,0]
	v_pk_fma_f32 v[184:185], v[184:185], 2.0, 1.0 op_sel_hi:[1,0,0]
	v_pk_fma_f32 v[186:187], v[186:187], 2.0, 1.0 op_sel_hi:[1,0,0]
	v_pk_fma_f32 v[240:241], v[240:241], 2.0, 1.0 op_sel_hi:[1,0,0]
	v_pk_fma_f32 v[242:243], v[242:243], 2.0, 1.0 op_sel_hi:[1,0,0]
	v_cvt_pk_bf16_f32 v154, v138, v139
	v_cvt_pk_bf16_f32 v155, v140, v141
	v_cvt_pk_bf16_f32 v156, v150, v151
	v_cvt_pk_bf16_f32 v157, v152, v153
	v_cvt_pk_bf16_f32 v158, v184, v185
	v_cvt_pk_bf16_f32 v159, v186, v187
	v_cvt_pk_bf16_f32 v160, v240, v241
	v_cvt_pk_bf16_f32 v161, v242, v243
	ds_read_b128 v[82:85], v172 offset:512
	ds_read_b128 v[34:37], v172 offset:576
	ds_read_b128 v[118:121], v172 offset:640
	ds_read_b128 v[46:49], v172 offset:704
	v_permlane16_swap_b32_e32 v154, v156
	v_permlane16_swap_b32_e32 v155, v157
	global_store_dwordx4 v228, v[154:157], s[64:65] nt
	v_permlane16_swap_b32_e32 v158, v160
	v_permlane16_swap_b32_e32 v159, v161
	global_store_dwordx4 v228, v[158:161], s[64:65] offset:128 nt
	v_log_f32_e32 v166, v162
	v_log_f32_e32 v167, v163
	v_log_f32_e32 v170, v174
	v_log_f32_e32 v171, v175
	v_add_f32_e32 v168, v164, v165
	v_mul_f32_e32 v168, 0xbeb17218, v168
	v_add_f32_e32 v166, v166, v167
	v_add_f32_e32 v170, v170, v171
	v_add_f32_e32 v166, v166, v170
	v_add_f32_e32 v166, 0xc2000000, v166
	v_fmac_f32_e32 v168, 0x3f317218, v166
	v_mov_b32_e32 v169, v168
	s_nop 1
	v_permlane16_swap_b32_e32 v168, v169
	v_add_f32_e32 v168, v168, v169
	v_mov_b32_e32 v169, v168
	s_nop 1
	v_permlane32_swap_b32_e32 v168, v169
	v_add_f32_e32 v168, v168, v169
	s_mov_b64 exec, s[0:1]
	global_store_dword v229, v168, s[66:67] offset:512
	s_mov_b64 exec, -1
	s_bitcmp1_b32 s20, 12
	s_cbranch_scc0 .Lg1_noY
	s_barrier
.Lg1_noY:
	v_exp_f32_e32 v130, v18
	v_exp_f32_e32 v131, v19
	v_exp_f32_e32 v132, v20
	v_exp_f32_e32 v133, v21
	v_exp_f32_e32 v142, v2
	v_exp_f32_e32 v143, v3
	v_exp_f32_e32 v144, v4
	v_exp_f32_e32 v145, v5
	v_exp_f32_e32 v176, v26
	v_exp_f32_e32 v177, v27
	v_exp_f32_e32 v178, v28
	v_exp_f32_e32 v179, v29
	v_exp_f32_e32 v232, v10
	v_exp_f32_e32 v233, v11
	v_exp_f32_e32 v234, v12
	v_exp_f32_e32 v235, v13
	v_pk_add_f32 v[130:131], v[130:131], 1.0 op_sel_hi:[1,0]
	v_pk_add_f32 v[132:133], v[132:133], 1.0 op_sel_hi:[1,0]
	v_pk_add_f32 v[142:143], v[142:143], 1.0 op_sel_hi:[1,0]
	v_pk_add_f32 v[144:145], v[144:145], 1.0 op_sel_hi:[1,0]
	v_pk_add_f32 v[176:177], v[176:177], 1.0 op_sel_hi:[1,0]
	v_pk_add_f32 v[178:179], v[178:179], 1.0 op_sel_hi:[1,0]
	v_pk_add_f32 v[232:233], v[232:233], 1.0 op_sel_hi:[1,0]
	v_pk_add_f32 v[234:235], v[234:235], 1.0 op_sel_hi:[1,0]
	v_pk_mul_f32 v[134:135], v[130:131], v[132:133]
	v_pk_mul_f32 v[146:147], v[142:143], v[144:145]
	v_pk_mul_f32 v[180:181], v[176:177], v[178:179]
	v_pk_mul_f32 v[236:237], v[232:233], v[234:235]
	v_rcp_f32_e64 v136, -v134
	v_rcp_f32_e64 v137, -v135
	v_rcp_f32_e64 v148, -v146
	v_rcp_f32_e64 v149, -v147
	v_rcp_f32_e64 v182, -v180
	v_rcp_f32_e64 v183, -v181
	v_rcp_f32_e64 v238, -v236
	v_rcp_f32_e64 v239, -v237
	v_pk_add_f32 v[164:165], v[18:19], v[20:21]
	v_pk_add_f32 v[164:165], v[164:165], v[2:3]
	v_pk_add_f32 v[164:165], v[164:165], v[4:5]
	v_pk_add_f32 v[164:165], v[164:165], v[26:27]
	v_pk_add_f32 v[164:165], v[164:165], v[28:29]
	v_pk_add_f32 v[164:165], v[164:165], v[10:11]
	v_pk_add_f32 v[164:165], v[164:165], v[12:13]
	v_pk_mul_f32 v[162:163], v[134:135], v[146:147]
	v_pk_mul_f32 v[162:163], v[162:163], v[180:181]
	v_pk_mul_f32 v[162:163], v[162:163], v[236:237]
	v_pk_mul_f32 v[140:141], v[136:137], v[130:131]
	v_pk_mul_f32 v[138:139], v[136:137], v[132:133]
	v_pk_mul_f32 v[152:153], v[148:149], v[142:143]
	v_pk_mul_f32 v[150:151], v[148:149], v[144:145]
	v_pk_mul_f32 v[186:187], v[182:183], v[176:177]
	v_pk_mul_f32 v[184:185], v[182:183], v[178:179]
	v_pk_mul_f32 v[242:243], v[238:239], v[232:233]
	v_pk_mul_f32 v[240:241], v[238:239], v[234:235]
	v_pk_fma_f32 v[138:139], v[138:139], 2.0, 1.0 op_sel_hi:[1,0,0]
	v_pk_fma_f32 v[140:141], v[140:141], 2.0, 1.0 op_sel_hi:[1,0,0]
	v_pk_fma_f32 v[150:151], v[150:151], 2.0, 1.0 op_sel_hi:[1,0,0]
	v_pk_fma_f32 v[152:153], v[152:153], 2.0, 1.0 op_sel_hi:[1,0,0]
	v_pk_fma_f32 v[184:185], v[184:185], 2.0, 1.0 op_sel_hi:[1,0,0]
	v_pk_fma_f32 v[186:187], v[186:187], 2.0, 1.0 op_sel_hi:[1,0,0]
	v_pk_fma_f32 v[240:241], v[240:241], 2.0, 1.0 op_sel_hi:[1,0,0]
	v_pk_fma_f32 v[242:243], v[242:243], 2.0, 1.0 op_sel_hi:[1,0,0]
	v_cvt_pk_bf16_f32 v154, v138, v139
	v_cvt_pk_bf16_f32 v155, v140, v141
	v_cvt_pk_bf16_f32 v156, v150, v151
	v_cvt_pk_bf16_f32 v157, v152, v153
	v_cvt_pk_bf16_f32 v158, v184, v185
	v_cvt_pk_bf16_f32 v159, v186, v187
	v_cvt_pk_bf16_f32 v160, v240, v241
	v_cvt_pk_bf16_f32 v161, v242, v243
	ds_read_b128 v[18:21], v172
	ds_read_b128 v[2:5], v172 offset:64
	ds_read_b128 v[26:29], v172 offset:128
	ds_read_b128 v[10:13], v172 offset:192
	v_permlane16_swap_b32_e32 v154, v156
	v_permlane16_swap_b32_e32 v155, v157
	global_store_dwordx4 v228, v[154:157], s[60:61] offset:2048 nt
	v_permlane16_swap_b32_e32 v158, v160
	v_permlane16_swap_b32_e32 v159, v161
	global_store_dwordx4 v228, v[158:161], s[60:61] offset:2176 nt
	v_exp_f32_e32 v130, v22
	v_exp_f32_e32 v131, v23
	v_exp_f32_e32 v132, v24
	v_exp_f32_e32 v133, v25
	v_exp_f32_e32 v142, v6
	v_exp_f32_e32 v143, v7
	v_exp_f32_e32 v144, v8
	v_exp_f32_e32 v145, v9
	v_exp_f32_e32 v176, v30
	v_exp_f32_e32 v177, v31
	v_exp_f32_e32 v178, v32
	v_exp_f32_e32 v179, v33
	v_exp_f32_e32 v232, v14
	v_exp_f32_e32 v233, v15
	v_exp_f32_e32 v234, v16
	v_exp_f32_e32 v235, v17
	v_pk_add_f32 v[130:131], v[130:131], 1.0 op_sel_hi:[1,0]
	v_pk_add_f32 v[132:133], v[132:133], 1.0 op_sel_hi:[1,0]
	v_pk_add_f32 v[142:143], v[142:143], 1.0 op_sel_hi:[1,0]
	v_pk_add_f32 v[144:145], v[144:145], 1.0 op_sel_hi:[1,0]
	v_pk_add_f32 v[176:177], v[176:177], 1.0 op_sel_hi:[1,0]
	v_pk_add_f32 v[178:179], v[178:179], 1.0 op_sel_hi:[1,0]
	v_pk_add_f32 v[232:233], v[232:233], 1.0 op_sel_hi:[1,0]
	v_pk_add_f32 v[234:235], v[234:235], 1.0 op_sel_hi:[1,0]
	v_pk_mul_f32 v[134:135], v[130:131], v[132:133]
	v_pk_mul_f32 v[146:147], v[142:143], v[144:145]
	v_pk_mul_f32 v[180:181], v[176:177], v[178:179]
	v_pk_mul_f32 v[236:237], v[232:233], v[234:235]
	v_rcp_f32_e64 v136, -v134
	v_rcp_f32_e64 v137, -v135
	v_rcp_f32_e64 v148, -v146
	v_rcp_f32_e64 v149, -v147
	v_rcp_f32_e64 v182, -v180
	v_rcp_f32_e64 v183, -v181
	v_rcp_f32_e64 v238, -v236
	v_rcp_f32_e64 v239, -v237
	v_pk_add_f32 v[164:165], v[164:165], v[22:23]
	v_pk_add_f32 v[164:165], v[164:165], v[24:25]
	v_pk_add_f32 v[164:165], v[164:165], v[6:7]
	v_pk_add_f32 v[164:165], v[164:165], v[8:9]
	v_pk_add_f32 v[164:165], v[164:165], v[30:31]
	v_pk_add_f32 v[164:165], v[164:165], v[32:33]
	v_pk_add_f32 v[164:165], v[164:165], v[14:15]
	v_pk_add_f32 v[164:165], v[164:165], v[16:17]
	v_pk_mul_f32 v[174:175], v[134:135], v[146:147]
	v_pk_mul_f32 v[174:175], v[174:175], v[180:181]
	v_pk_mul_f32 v[174:175], v[174:175], v[236:237]
	v_pk_mul_f32 v[140:141], v[136:137], v[130:131]
	v_pk_mul_f32 v[138:139], v[136:137], v[132:133]
	v_pk_mul_f32 v[152:153], v[148:149], v[142:143]
	v_pk_mul_f32 v[150:151], v[148:149], v[144:145]
	v_pk_mul_f32 v[186:187], v[182:183], v[176:177]
	v_pk_mul_f32 v[184:185], v[182:183], v[178:179]
	v_pk_mul_f32 v[242:243], v[238:239], v[232:233]
	v_pk_mul_f32 v[240:241], v[238:239], v[234:235]
	v_pk_fma_f32 v[138:139], v[138:139], 2.0, 1.0 op_sel_hi:[1,0,0]
	v_pk_fma_f32 v[140:141], v[140:141], 2.0, 1.0 op_sel_hi:[1,0,0]
	v_pk_fma_f32 v[150:151], v[150:151], 2.0, 1.0 op_sel_hi:[1,0,0]
	v_pk_fma_f32 v[152:153], v[152:153], 2.0, 1.0 op_sel_hi:[1,0,0]
	v_pk_fma_f32 v[184:185], v[184:185], 2.0, 1.0 op_sel_hi:[1,0,0]
	v_pk_fma_f32 v[186:187], v[186:187], 2.0, 1.0 op_sel_hi:[1,0,0]
	v_pk_fma_f32 v[240:241], v[240:241], 2.0, 1.0 op_sel_hi:[1,0,0]
	v_pk_fma_f32 v[242:243], v[242:243], 2.0, 1.0 op_sel_hi:[1,0,0]
	v_cvt_pk_bf16_f32 v154, v138, v139
	v_cvt_pk_bf16_f32 v155, v140, v141
	v_cvt_pk_bf16_f32 v156, v150, v151
	v_cvt_pk_bf16_f32 v157, v152, v153
	v_cvt_pk_bf16_f32 v158, v184, v185
	v_cvt_pk_bf16_f32 v159, v186, v187
	v_cvt_pk_bf16_f32 v160, v240, v241
	v_cvt_pk_bf16_f32 v161, v242, v243
	ds_read_b128 v[22:25], v172 offset:512
	ds_read_b128 v[6:9], v172 offset:576
	ds_read_b128 v[30:33], v172 offset:640
	ds_read_b128 v[14:17], v172 offset:704
	v_permlane16_swap_b32_e32 v154, v156
	v_permlane16_swap_b32_e32 v155, v157
	global_store_dwordx4 v228, v[154:157], s[64:65] offset:2048 nt
	v_permlane16_swap_b32_e32 v158, v160
	v_permlane16_swap_b32_e32 v159, v161
	global_store_dwordx4 v228, v[158:161], s[64:65] offset:2176 nt
	v_log_f32_e32 v166, v162
	v_log_f32_e32 v167, v163
	v_log_f32_e32 v170, v174
	v_log_f32_e32 v171, v175
	v_add_f32_e32 v168, v164, v165
	v_mul_f32_e32 v168, 0xbeb17218, v168
	v_add_f32_e32 v166, v166, v167
	v_add_f32_e32 v170, v170, v171
	v_add_f32_e32 v166, v166, v170
	v_add_f32_e32 v166, 0xc2000000, v166
	v_fmac_f32_e32 v168, 0x3f317218, v166
	v_mov_b32_e32 v169, v168
	s_nop 1
	v_permlane16_swap_b32_e32 v168, v169
	v_add_f32_e32 v168, v168, v169
	v_mov_b32_e32 v169, v168
	s_nop 1
	v_permlane32_swap_b32_e32 v168, v169
	v_add_f32_e32 v168, v168, v169
	s_mov_b64 exec, s[0:1]
	global_store_dword v229, v168, s[66:67] offset:576
	s_mov_b64 exec, -1
	s_mov_b64 s[2:3], 0
	s_branch .LBB3_5

	.amdhsa_kernel _Z7gemm1_kPKDF16_S0_PDF16_PKfPfS0_S1_
		.amdhsa_group_segment_fixed_size 0
		.amdhsa_private_segment_fixed_size 0
		.amdhsa_kernarg_size 56
		.amdhsa_user_sgpr_count 2
		.amdhsa_user_sgpr_dispatch_ptr 0
		.amdhsa_user_sgpr_queue_ptr 0
		.amdhsa_user_sgpr_kernarg_segment_ptr 1
		.amdhsa_user_sgpr_dispatch_id 0
		.amdhsa_user_sgpr_kernarg_preload_length 0
		.amdhsa_user_sgpr_kernarg_preload_offset 0
		.amdhsa_user_sgpr_private_segment_size 0
		.amdhsa_uses_dynamic_stack 0
		.amdhsa_enable_private_segment 0
		.amdhsa_system_sgpr_workgroup_id_x 1
		.amdhsa_system_sgpr_workgroup_id_y 0
		.amdhsa_system_sgpr_workgroup_id_z 0
		.amdhsa_system_sgpr_workgroup_info 0
		.amdhsa_system_vgpr_workitem_id 0
		.amdhsa_next_free_vgpr 244
		.amdhsa_next_free_sgpr 68
		.amdhsa_accum_offset 244
		.amdhsa_reserve_vcc 1
		.amdhsa_float_round_mode_32 0
		.amdhsa_float_round_mode_16_64 0
		.amdhsa_float_denorm_mode_32 3
		.amdhsa_float_denorm_mode_16_64 3
		.amdhsa_dx10_clamp 1
		.amdhsa_ieee_mode 1
		.amdhsa_fp16_overflow 0
		.amdhsa_tg_split 0
		.amdhsa_exception_fp_ieee_invalid_op 0
		.amdhsa_exception_fp_denorm_src 0
		.amdhsa_exception_fp_ieee_div_zero 0
		.amdhsa_exception_fp_ieee_overflow 0
		.amdhsa_exception_fp_ieee_underflow 0
		.amdhsa_exception_fp_ieee_inexact 0
		.amdhsa_exception_int_div_zero 0
	.end_amdhsa_kernel

amdhsa.kernels:
  - .agpr_count:     0
    .args:
      - .actual_access:  read_only
        .address_space:  global
        .offset:         0
        .size:           8
        .value_kind:     global_buffer
      - .actual_access:  read_only
        .address_space:  global
        .offset:         8
        .size:           8
        .value_kind:     global_buffer
      - .actual_access:  read_only
        .address_space:  global
        .offset:         16
        .size:           8
        .value_kind:     global_buffer
      - .actual_access:  write_only
        .address_space:  global
        .offset:         24
        .size:           8
        .value_kind:     global_buffer
      - .actual_access:  write_only
        .address_space:  global
        .offset:         32
        .size:           8
        .value_kind:     global_buffer
      - .actual_access:  write_only
        .address_space:  global
        .offset:         40
        .size:           8
        .value_kind:     global_buffer
      - .actual_access:  write_only
        .address_space:  global
        .offset:         48
        .size:           8
        .value_kind:     global_buffer
      - .actual_access:  read_only
        .address_space:  global
        .offset:         56
        .size:           8
        .value_kind:     global_buffer
      - .actual_access:  read_only
        .address_space:  global
        .offset:         64
        .size:           8
        .value_kind:     global_buffer
      - .actual_access:  write_only
        .address_space:  global
        .offset:         72
        .size:           8
        .value_kind:     global_buffer
    .group_segment_fixed_size: 8448
    .kernarg_segment_align: 8
    .kernarg_segment_size: 80
    .language:       OpenCL C
    .language_version:
      - 2
      - 0
    .max_flat_workgroup_size: 256
    .name:           _Z6prep_kPKfS0_S0_PDF16_S1_S1_S1_S1_S0_Pf
    .private_segment_fixed_size: 0
    .sgpr_count:     22
    .sgpr_spill_count: 0
    .symbol:         _Z6prep_kPKfS0_S0_PDF16_S1_S1_S1_S1_S0_Pf.kd
    .uniform_work_group_size: 1
    .uses_dynamic_stack: false
    .vgpr_count:     34
    .vgpr_spill_count: 0
    .wavefront_size: 64
  - .agpr_count:     0
    .args:
      - .actual_access:  read_only
        .address_space:  global
        .offset:         0
        .size:           8
        .value_kind:     global_buffer
      - .actual_access:  write_only
        .address_space:  global
        .offset:         8
        .size:           8
        .value_kind:     global_buffer
      - .actual_access:  read_only
        .address_space:  global
        .offset:         16
        .size:           8
        .value_kind:     global_buffer
      - .actual_access:  write_only
        .address_space:  global
        .offset:         24
        .size:           8
        .value_kind:     global_buffer
      - .offset:         32
        .size:           4
        .value_kind:     hidden_block_count_x
      - .offset:         36
        .size:           4
        .value_kind:     hidden_block_count_y
      - .offset:         40
        .size:           4
        .value_kind:     hidden_block_count_z
      - .offset:         44
        .size:           2
        .value_kind:     hidden_group_size_x
      - .offset:         46
        .size:           2
        .value_kind:     hidden_group_size_y
      - .offset:         48
        .size:           2
        .value_kind:     hidden_group_size_z
      - .offset:         50
        .size:           2
        .value_kind:     hidden_remainder_x
      - .offset:         52
        .size:           2
        .value_kind:     hidden_remainder_y
      - .offset:         54
        .size:           2
        .value_kind:     hidden_remainder_z
      - .offset:         72
        .size:           8
        .value_kind:     hidden_global_offset_x
      - .offset:         80
        .size:           8
        .value_kind:     hidden_global_offset_y
      - .offset:         88
        .size:           8
        .value_kind:     hidden_global_offset_z
      - .offset:         96
        .size:           2
        .value_kind:     hidden_grid_dims
    .group_segment_fixed_size: 0
    .kernarg_segment_align: 8
    .kernarg_segment_size: 288
    .language:       OpenCL C
    .language_version:
      - 2
      - 0
    .max_flat_workgroup_size: 1024
    .name:           _Z6post_kPKfPfPKDF16_PDF16_
    .private_segment_fixed_size: 0
    .sgpr_count:     14
    .sgpr_spill_count: 0
    .symbol:         _Z6post_kPKfPfPKDF16_PDF16_.kd
    .uniform_work_group_size: 1
    .uses_dynamic_stack: false
    .vgpr_count:     49
    .vgpr_spill_count: 0
    .wavefront_size: 64
  - .agpr_count:     0
    .args:
      - .actual_access:  read_only
        .address_space:  global
        .offset:         0
        .size:           8
        .value_kind:     global_buffer
      - .actual_access:  read_only
        .address_space:  global
        .offset:         8
        .size:           8
        .value_kind:     global_buffer
      - .actual_access:  write_only
        .address_space:  global
        .offset:         16
        .size:           8
        .value_kind:     global_buffer
      - .offset:         24
        .size:           4
        .value_kind:     hidden_block_count_x
      - .offset:         28
        .size:           4
        .value_kind:     hidden_block_count_y
      - .offset:         32
        .size:           4
        .value_kind:     hidden_block_count_z
      - .offset:         36
        .size:           2
        .value_kind:     hidden_group_size_x
      - .offset:         38
        .size:           2
        .value_kind:     hidden_group_size_y
      - .offset:         40
        .size:           2
        .value_kind:     hidden_group_size_z
      - .offset:         42
        .size:           2
        .value_kind:     hidden_remainder_x
      - .offset:         44
        .size:           2
        .value_kind:     hidden_remainder_y
      - .offset:         46
        .size:           2
        .value_kind:     hidden_remainder_z
      - .offset:         64
        .size:           8
        .value_kind:     hidden_global_offset_x
      - .offset:         72
        .size:           8
        .value_kind:     hidden_global_offset_y
      - .offset:         80
        .size:           8
        .value_kind:     hidden_global_offset_z
      - .offset:         88
        .size:           2
        .value_kind:     hidden_grid_dims
    .group_segment_fixed_size: 0
    .kernarg_segment_align: 8
    .kernarg_segment_size: 280
    .language:       OpenCL C
    .language_version:
      - 2
      - 0
    .max_flat_workgroup_size: 1024
    .name:           _Z8reduce_kPKDF16_PKfPf
    .private_segment_fixed_size: 0
    .sgpr_count:     16
    .sgpr_spill_count: 0
    .symbol:         _Z8reduce_kPKDF16_PKfPf.kd
    .uniform_work_group_size: 1
    .uses_dynamic_stack: false
    .vgpr_count:     42
    .vgpr_spill_count: 0
    .wavefront_size: 64
  - .agpr_count:     0
    .args:
      - .actual_access:  read_only
        .address_space:  global
        .offset:         0
        .size:           8
        .value_kind:     global_buffer
      - .actual_access:  read_only
        .address_space:  global
        .offset:         8
        .size:           8
        .value_kind:     global_buffer
      - .actual_access:  write_only
        .address_space:  global
        .offset:         16
        .size:           8
        .value_kind:     global_buffer
      - .address_space:  global
        .offset:         24
        .size:           8
        .value_kind:     global_buffer
      - .actual_access:  write_only
        .address_space:  global
        .offset:         32
        .size:           8
        .value_kind:     global_buffer
      - .actual_access:  read_only
        .address_space:  global
        .offset:         40
        .size:           8
        .value_kind:     global_buffer
      - .actual_access:  write_only
        .address_space:  global
        .offset:         48
        .size:           8
        .value_kind:     global_buffer
    .group_segment_fixed_size: 0
    .kernarg_segment_align: 8
    .kernarg_segment_size: 56
    .language:       OpenCL C
    .language_version:
      - 2
      - 0
    .max_flat_workgroup_size: 512
    .name:           _Z7gemm1_kPKDF16_S0_PDF16_PKfPfS0_S1_
    .private_segment_fixed_size: 0
    .sgpr_count:     74
    .sgpr_spill_count: 0
    .symbol:         _Z7gemm1_kPKDF16_S0_PDF16_PKfPfS0_S1_.kd
    .uniform_work_group_size: 1
    .uses_dynamic_stack: false
    .vgpr_count:     244
    .vgpr_spill_count: 0
    .wavefront_size: 64
  - .agpr_count:     0
    .args:
      - .actual_access:  read_only
        .address_space:  global
        .offset:         0
        .size:           8
        .value_kind:     global_buffer
      - .actual_access:  read_only
        .address_space:  global
        .offset:         8
        .size:           8
        .value_kind:     global_buffer
      - .offset:         16
        .size:           4
        .value_kind:     by_value
      - .offset:         20
        .size:           4
        .value_kind:     by_value
      - .offset:         24
        .size:           4
        .value_kind:     by_value
      - .offset:         28
        .size:           4
        .value_kind:     by_value
      - .actual_access:  read_only
        .address_space:  global
        .offset:         32
        .size:           8
        .value_kind:     global_buffer
      - .actual_access:  write_only
        .address_space:  global
        .offset:         40
        .size:           8
        .value_kind:     global_buffer
      - .actual_access:  read_only
        .address_space:  global
        .offset:         48
        .size:           8
        .value_kind:     global_buffer
      - .actual_access:  read_only
        .address_space:  global
        .offset:         56
        .size:           8
        .value_kind:     global_buffer
    .group_segment_fixed_size: 0
    .kernarg_segment_align: 8
    .kernarg_segment_size: 64
    .language:       OpenCL C
    .language_version:
      - 2
      - 0
    .max_flat_workgroup_size: 512
    .name:           _Z6gemm_kILi2EEvPKDF16_S1_iiiiPfPDF16_PKfS2_
    .private_segment_fixed_size: 0
    .sgpr_count:     70
    .sgpr_spill_count: 0
    .symbol:         _Z6gemm_kILi2EEvPKDF16_S1_iiiiPfPDF16_PKfS2_.kd
    .uniform_work_group_size: 1
    .uses_dynamic_stack: false
    .vgpr_count:     224
    .vgpr_spill_count: 0
    .wavefront_size: 64
  - .agpr_count:     0
    .args:
      - .actual_access:  read_only
        .address_space:  global
        .offset:         0
        .size:           8
        .value_kind:     global_buffer
      - .actual_access:  read_only
        .address_space:  global
        .offset:         8
        .size:           8
        .value_kind:     global_buffer
      - .offset:         16
        .size:           4
        .value_kind:     by_value
      - .offset:         20
        .size:           4
        .value_kind:     by_value
      - .offset:         24
        .size:           4
        .value_kind:     by_value
      - .offset:         28
        .size:           4
        .value_kind:     by_value
      - .actual_access:  read_only
        .address_space:  global
        .offset:         32
        .size:           8
        .value_kind:     global_buffer
      - .actual_access:  write_only
        .address_space:  global
        .offset:         40
        .size:           8
        .value_kind:     global_buffer
      - .actual_access:  read_only
        .address_space:  global
        .offset:         48
        .size:           8
        .value_kind:     global_buffer
      - .actual_access:  read_only
        .address_space:  global
        .offset:         56
        .size:           8
        .value_kind:     global_buffer
    .group_segment_fixed_size: 0
    .kernarg_segment_align: 8
    .kernarg_segment_size: 64
    .language:       OpenCL C
    .language_version:
      - 2
      - 0
    .max_flat_workgroup_size: 512
    .name:           _Z6gemm_kILi3EEvPKDF16_S1_iiiiPfPDF16_PKfS2_
    .private_segment_fixed_size: 0
    .sgpr_count:     51
    .sgpr_spill_count: 0
    .symbol:         _Z6gemm_kILi3EEvPKDF16_S1_iiiiPfPDF16_PKfS2_.kd
    .uniform_work_group_size: 1
    .uses_dynamic_stack: false
    .vgpr_count:     220
    .vgpr_spill_count: 0
    .wavefront_size: 64
